# P5 m3 unit: q.n_prev rows and stage-1 q fragments also read from the LDS q tile (no global q loads left in the unit after staging)
# speedup vs baseline: 1.0211x; 1.0034x over previous
.LBB0_767:
	s_or_b64 exec, exec, s[60:61]
	s_waitcnt vmcnt(0)
	v_lshl_add_u64 v[0:1], s[54:55], 0, v[116:117]
	s_lshl_b32 s49, s49, 7
	v_lshlrev_b64 v[0:1], 10, v[0:1]
	v_lshl_add_u64 v[0:1], s[0:1], 0, v[0:1]
	s_lshl_b32 s96, s49, 1
	v_lshl_add_u64 v[0:1], v[0:1], 0, s[96:97]
	v_mov_b32_e32 v139, v85
	v_lshl_add_u64 v[4:5], v[0:1], 0, v[138:139]
	v_mbcnt_lo_u32_b32 v244, -1, 0
	v_mbcnt_hi_u32_b32 v244, -1, v244
	v_readlane_b32 s32, v252, 1
	s_lshl_b32 s32, s32, 6
	v_add_u32_e32 v244, s32, v244
	v_lshrrev_b32_e32 v245, 2, v244
	v_and_b32_e32 v244, 3, v244
	v_mul_u32_u24_e32 v245, 0x110, v245
	v_lshl_add_u32 v244, v244, 6, v245
	v_add_u32_e32 v244, 0x1b810, v244
	ds_read_b128 v[0:3], v244 offset:48
	ds_read_b128 v[6:9], v244 offset:32
	ds_read_b128 v[10:13], v244 offset:16
	ds_read_b128 v[14:17], v244
	s_waitcnt vmcnt(0)
	s_waitcnt lgkmcnt(0)
	v_lshlrev_b32_e32 v4, 16, v14
	v_and_b32_e32 v5, 0xffff0000, v14
	v_lshlrev_b32_e32 v30, 16, v15
	v_and_b32_e32 v31, 0xffff0000, v15
	v_lshlrev_b32_e32 v32, 16, v16
	v_and_b32_e32 v33, 0xffff0000, v16
	v_lshlrev_b32_e32 v34, 16, v17
	v_and_b32_e32 v35, 0xffff0000, v17
	ds_read_b128 v[14:17], v194
	ds_read_b128 v[18:21], v194 offset:16
	ds_read_b128 v[22:25], v194 offset:32
	ds_read_b128 v[26:29], v194 offset:48
	s_waitcnt lgkmcnt(3)
	v_fma_f32 v4, v14, v4, 0
	v_fmac_f32_e32 v4, v15, v5
	v_fmac_f32_e32 v4, v16, v30
	v_fmac_f32_e32 v4, v17, v31
	s_waitcnt lgkmcnt(2)
	v_fmac_f32_e32 v4, v18, v32
	v_fmac_f32_e32 v4, v19, v33
	v_fmac_f32_e32 v4, v20, v34
	v_fmac_f32_e32 v4, v21, v35
	v_lshlrev_b32_e32 v5, 16, v10
	v_and_b32_e32 v10, 0xffff0000, v10
	s_waitcnt lgkmcnt(1)
	v_fmac_f32_e32 v4, v22, v5
	v_lshlrev_b32_e32 v14, 16, v11
	v_fmac_f32_e32 v4, v23, v10
	v_and_b32_e32 v11, 0xffff0000, v11
	v_fmac_f32_e32 v4, v24, v14
	v_lshlrev_b32_e32 v15, 16, v12
	v_fmac_f32_e32 v4, v25, v11
	v_and_b32_e32 v12, 0xffff0000, v12
	s_waitcnt lgkmcnt(0)
	v_fmac_f32_e32 v4, v26, v15
	v_lshlrev_b32_e32 v16, 16, v13
	v_fmac_f32_e32 v4, v27, v12
	v_and_b32_e32 v13, 0xffff0000, v13
	v_fmac_f32_e32 v4, v28, v16
	v_fmac_f32_e32 v4, v29, v13
	v_lshlrev_b32_e32 v5, 16, v6
	v_and_b32_e32 v10, 0xffff0000, v6
	v_lshlrev_b32_e32 v11, 16, v7
	v_and_b32_e32 v12, 0xffff0000, v7
	v_lshlrev_b32_e32 v13, 16, v8
	v_and_b32_e32 v14, 0xffff0000, v8
	v_lshlrev_b32_e32 v15, 16, v9
	v_and_b32_e32 v16, 0xffff0000, v9
	ds_read_b128 v[6:9], v194 offset:64
	s_waitcnt lgkmcnt(0)
	v_fmac_f32_e32 v4, v6, v5
	v_fmac_f32_e32 v4, v7, v10
	v_fmac_f32_e32 v4, v8, v11
	v_fmac_f32_e32 v4, v9, v12
	ds_read_b128 v[6:9], v194 offset:80
	v_lshlrev_b32_e32 v5, 16, v0
	v_and_b32_e32 v10, 0xffff0000, v2
	v_lshlrev_b32_e32 v11, 16, v3
	v_and_b32_e32 v12, 0xffff0000, v3
	s_waitcnt lgkmcnt(0)
	v_fmac_f32_e32 v4, v6, v13
	v_fmac_f32_e32 v4, v7, v14
	v_fmac_f32_e32 v4, v8, v15
	v_fmac_f32_e32 v4, v9, v16
	v_and_b32_e32 v6, 0xffff0000, v0
	v_lshlrev_b32_e32 v7, 16, v1
	v_and_b32_e32 v8, 0xffff0000, v1
	v_lshlrev_b32_e32 v9, 16, v2
	ds_read_b128 v[0:3], v194 offset:96
	s_waitcnt lgkmcnt(0)
	v_fmac_f32_e32 v4, v0, v5
	v_fmac_f32_e32 v4, v1, v6
	v_fmac_f32_e32 v4, v2, v7
	v_fmac_f32_e32 v4, v3, v8
	ds_read_b128 v[0:3], v194 offset:112
	s_waitcnt lgkmcnt(0)
	v_fmac_f32_e32 v4, v0, v9
	v_fmac_f32_e32 v4, v1, v10
	v_fmac_f32_e32 v4, v2, v11
	v_fmac_f32_e32 v4, v3, v12
	ds_bpermute_b32 v0, v158, v4
	s_waitcnt lgkmcnt(0)
	v_add_f32_e32 v0, v4, v0
	ds_bpermute_b32 v1, v159, v0
	s_and_saveexec_b64 s[60:61], s[14:15]
	s_cbranch_execz .LBB0_769
	s_waitcnt lgkmcnt(0)
	v_add_f32_e32 v0, v0, v1
	ds_write_b32 v173, v0
.LBB0_769:
	s_or_b64 exec, exec, s[60:61]
	s_waitcnt lgkmcnt(0)
	v_lshl_add_u64 v[0:1], s[54:55], 0, v[118:119]
	v_lshlrev_b64 v[0:1], 10, v[0:1]
	v_lshl_add_u64 v[0:1], s[0:1], 0, v[0:1]
	v_lshl_add_u64 v[0:1], v[0:1], 0, s[96:97]
	v_mov_b32_e32 v141, v85
	v_lshl_add_u64 v[0:1], v[0:1], 0, v[140:141]
	s_barrier
	v_mbcnt_lo_u32_b32 v246, -1, 0
	v_mbcnt_hi_u32_b32 v246, -1, v246
	v_and_b32_e32 v247, 15, v246
	v_lshrrev_b32_e32 v246, 4, v246
	v_lshlrev_b32_e32 v246, 4, v246
	v_readlane_b32 s32, v252, 1
	s_lshl_b32 s32, s32, 4
	v_add_u32_e32 v247, s32, v247
	v_mul_u32_u24_e32 v247, 0x110, v247
	v_add_u32_e32 v246, v246, v247
	v_add_u32_e32 v246, 0x1b810, v246
	ds_read_b128 v[12:15], v246
	ds_read_b128 v[8:11], v246 offset:64
	ds_read_b128 v[4:7], v246 offset:128
	s_nop 0
	ds_read_b128 v[0:3], v246 offset:192
	ds_read_b32 v36, v162
	ds_read_b128 v[16:19], v197
	ds_read_b128 v[20:23], v197 offset:64
	v_readlane_b32 s60, v253, 4
	v_readlane_b32 s61, v253, 5
	s_waitcnt vmcnt(3) lgkmcnt(1)
	v_mfma_f32_16x16x32_bf16 v[16:19], v[16:19], v[12:15], 0
	s_waitcnt vmcnt(2) lgkmcnt(0)
	v_mfma_f32_16x16x32_bf16 v[16:19], v[20:23], v[8:11], v[16:19]
	ds_read_b128 v[20:23], v197 offset:128
	s_waitcnt vmcnt(1) lgkmcnt(0)
	v_mfma_f32_16x16x32_bf16 v[16:19], v[20:23], v[4:7], v[16:19]
	ds_read_b128 v[20:23], v197 offset:192
	s_waitcnt vmcnt(0) lgkmcnt(0)
	v_mfma_f32_16x16x32_bf16 v[16:19], v[20:23], v[0:3], v[16:19]
	ds_read_b128 v[20:23], v163
	s_waitcnt lgkmcnt(0)
	v_sub_f32_e32 v20, v20, v36
	v_mul_f32_e32 v24, 0x3fb8aa3b, v20
	v_fma_f32 v25, v20, s67, -v24
	v_rndne_f32_e32 v26, v24
	v_fmac_f32_e32 v25, 0x32a5705f, v20
	v_sub_f32_e32 v24, v24, v26
	v_add_f32_e32 v24, v24, v25
	v_exp_f32_e32 v24, v24
	v_cvt_i32_f32_e32 v25, v26
	v_cmp_ngt_f32_e32 vcc, s68, v20
	v_sub_f32_e32 v21, v21, v36
	v_ldexp_f32 v24, v24, v25
	v_cndmask_b32_e32 v24, 0, v24, vcc
	v_cmp_nlt_f32_e32 vcc, s69, v20
	s_nop 1
	v_cndmask_b32_e32 v20, v196, v24, vcc
	v_mul_f32_e32 v24, 0x3fb8aa3b, v21
	v_fma_f32 v25, v21, s67, -v24
	v_rndne_f32_e32 v26, v24
	v_fmac_f32_e32 v25, 0x32a5705f, v21
	v_sub_f32_e32 v24, v24, v26
	v_add_f32_e32 v24, v24, v25
	v_exp_f32_e32 v24, v24
	v_cvt_i32_f32_e32 v25, v26
	v_cmp_ngt_f32_e32 vcc, s68, v21
	v_ldexp_f32 v24, v24, v25
	s_nop 0
	v_cndmask_b32_e32 v24, 0, v24, vcc
	v_cmp_nlt_f32_e32 vcc, s69, v21
	v_sub_f32_e32 v21, v22, v36
	v_mul_f32_e32 v22, 0x3fb8aa3b, v21
	v_fma_f32 v25, v21, s67, -v22
	v_rndne_f32_e32 v26, v22
	v_fmac_f32_e32 v25, 0x32a5705f, v21
	v_sub_f32_e32 v22, v22, v26
	v_add_f32_e32 v22, v22, v25
	v_exp_f32_e32 v22, v22
	v_cvt_i32_f32_e32 v25, v26
	v_cndmask_b32_e32 v24, v196, v24, vcc
	v_cmp_ngt_f32_e32 vcc, s68, v21
	v_ldexp_f32 v22, v22, v25
	s_nop 0
	v_cndmask_b32_e32 v22, 0, v22, vcc
	v_cmp_nlt_f32_e32 vcc, s69, v21
	s_nop 1
	v_cndmask_b32_e32 v21, v196, v22, vcc
	v_sub_f32_e32 v22, v23, v36
	v_mul_f32_e32 v23, 0x3fb8aa3b, v22
	v_fma_f32 v25, v22, s67, -v23
	v_rndne_f32_e32 v26, v23
	v_fmac_f32_e32 v25, 0x32a5705f, v22
	v_sub_f32_e32 v23, v23, v26
	v_add_f32_e32 v23, v23, v25
	v_exp_f32_e32 v23, v23
	v_cvt_i32_f32_e32 v25, v26
	v_cmp_ngt_f32_e32 vcc, s68, v22
	v_ldexp_f32 v23, v23, v25
	s_nop 0
	v_cndmask_b32_e32 v23, 0, v23, vcc
	v_cmp_nlt_f32_e32 vcc, s69, v22
	v_mov_b32_e32 v22, v16
	s_nop 0
	v_cndmask_b32_e32 v25, v196, v23, vcc
	v_mov_b32_e32 v23, v18
	v_pk_mul_f32 v[20:21], v[22:23], v[20:21]
	v_mov_b32_e32 v18, v17
	v_cndmask_b32_e64 v33, v20, 0, s[24:25]
	v_pk_mul_f32 v[16:17], v[18:19], v[24:25]
	v_add_f32_e32 v20, 0, v33
	v_cndmask_b32_e64 v35, v16, 0, s[28:29]
	v_cndmask_b32_e64 v32, v21, 0, s[22:23]
	v_add_f32_e32 v16, v35, v20
	v_cndmask_b32_e64 v34, v17, 0, s[26:27]
	v_add_f32_e32 v16, v32, v16
	v_add_f32_e32 v37, v34, v16
	v_mov_b32_e32 v20, 0
	s_andn2_b64 vcc, exec, s[60:61]
	s_cbranch_vccnz .LBB0_777
	ds_read_b128 v[16:19], v197 offset:4352
	ds_read_b128 v[22:25], v197 offset:4416
	v_readlane_b32 s60, v252, 4
	v_readlane_b32 s61, v252, 5
	s_waitcnt lgkmcnt(1)
	v_mfma_f32_16x16x32_bf16 v[16:19], v[16:19], v[12:15], 0
	s_waitcnt lgkmcnt(0)
	v_mfma_f32_16x16x32_bf16 v[16:19], v[22:25], v[8:11], v[16:19]
	ds_read_b128 v[22:25], v197 offset:4480
	s_waitcnt lgkmcnt(0)
	v_mfma_f32_16x16x32_bf16 v[16:19], v[22:25], v[4:7], v[16:19]
	ds_read_b128 v[22:25], v197 offset:4544
	s_waitcnt lgkmcnt(0)
	v_mfma_f32_16x16x32_bf16 v[16:19], v[22:25], v[0:3], v[16:19]
	ds_read_b128 v[22:25], v163 offset:64
	s_waitcnt lgkmcnt(0)
	v_sub_f32_e32 v21, v22, v36
	v_mul_f32_e32 v22, 0x3fb8aa3b, v21
	v_fma_f32 v26, v21, s67, -v22
	v_rndne_f32_e32 v27, v22
	v_fmac_f32_e32 v26, 0x32a5705f, v21
	v_sub_f32_e32 v22, v22, v27
	v_add_f32_e32 v22, v22, v26
	v_exp_f32_e32 v22, v22
	v_cvt_i32_f32_e32 v26, v27
	v_cmp_ngt_f32_e32 vcc, s68, v21
	v_ldexp_f32 v22, v22, v26
	s_nop 0
	v_cndmask_b32_e32 v22, 0, v22, vcc
	v_cmp_nlt_f32_e32 vcc, s69, v21
	v_sub_f32_e32 v21, v23, v36
	v_mul_f32_e32 v23, 0x3fb8aa3b, v21
	v_fma_f32 v26, v21, s67, -v23
	v_rndne_f32_e32 v27, v23
	v_fmac_f32_e32 v26, 0x32a5705f, v21
	v_sub_f32_e32 v23, v23, v27
	v_add_f32_e32 v23, v23, v26
	v_exp_f32_e32 v23, v23
	v_cvt_i32_f32_e32 v26, v27
	v_cndmask_b32_e32 v22, v196, v22, vcc
	v_cmp_ngt_f32_e32 vcc, s68, v21
	v_ldexp_f32 v23, v23, v26
	s_nop 0
	v_cndmask_b32_e32 v23, 0, v23, vcc
	v_cmp_nlt_f32_e32 vcc, s69, v21
	v_sub_f32_e32 v21, v24, v36
	v_mul_f32_e32 v24, 0x3fb8aa3b, v21
	v_fma_f32 v26, v21, s67, -v24
	v_rndne_f32_e32 v27, v24
	v_fmac_f32_e32 v26, 0x32a5705f, v21
	v_sub_f32_e32 v24, v24, v27
	v_add_f32_e32 v24, v24, v26
	v_exp_f32_e32 v24, v24
	v_cvt_i32_f32_e32 v26, v27
	v_cndmask_b32_e32 v23, v196, v23, vcc
	v_cmp_ngt_f32_e32 vcc, s68, v21
	v_pk_mul_f32 v[16:17], v[16:17], v[22:23]
	v_ldexp_f32 v24, v24, v26
	v_cndmask_b32_e32 v24, 0, v24, vcc
	v_cmp_nlt_f32_e32 vcc, s69, v21
	v_sub_f32_e32 v21, v25, v36
	v_mul_f32_e32 v25, 0x3fb8aa3b, v21
	v_fma_f32 v26, v21, s67, -v25
	v_rndne_f32_e32 v27, v25
	v_fmac_f32_e32 v26, 0x32a5705f, v21
	v_sub_f32_e32 v25, v25, v27
	v_add_f32_e32 v25, v25, v26
	v_exp_f32_e32 v25, v25
	v_cvt_i32_f32_e32 v26, v27
	v_cndmask_b32_e64 v17, v17, 0, s[60:61]
	v_readlane_b32 s60, v252, 6
	v_readlane_b32 s61, v252, 7
	v_cndmask_b32_e32 v24, v196, v24, vcc
	v_ldexp_f32 v25, v25, v26
	v_cndmask_b32_e64 v16, v16, 0, s[60:61]
	v_cmp_ngt_f32_e32 vcc, s68, v21
	v_and_b32_sdwa v23, v16, v198 dst_sel:DWORD dst_unused:UNUSED_PAD src0_sel:WORD_1 src1_sel:DWORD
	v_and_b32_sdwa v22, v17, v198 dst_sel:DWORD dst_unused:UNUSED_PAD src0_sel:WORD_1 src1_sel:DWORD
	v_cndmask_b32_e32 v25, 0, v25, vcc
	v_cmp_nlt_f32_e32 vcc, s69, v21
	v_add_f32_e32 v21, v37, v16
	v_add3_u32 v16, v16, v23, s71
	v_cndmask_b32_e32 v25, v196, v25, vcc
	v_add_f32_e32 v21, v17, v21
	v_add3_u32 v17, v17, v22, s71
	v_lshrrev_b32_e32 v16, 16, v16
	v_readlane_b32 s60, v252, 8
	v_and_or_b32 v22, v17, s70, v16
	v_pk_mul_f32 v[16:17], v[18:19], v[24:25]
	v_readlane_b32 s61, v252, 9
	s_nop 1
	v_cndmask_b32_e64 v17, v17, 0, s[60:61]
	v_readlane_b32 s60, v252, 10
	v_readlane_b32 s61, v252, 11
	s_nop 1
	v_cndmask_b32_e64 v16, v16, 0, s[60:61]
	v_add_f32_e32 v18, v16, v21
	v_and_b32_sdwa v19, v16, v198 dst_sel:DWORD dst_unused:UNUSED_PAD src0_sel:WORD_1 src1_sel:DWORD
	v_add_f32_e32 v37, v17, v18
	v_and_b32_sdwa v18, v17, v198 dst_sel:DWORD dst_unused:UNUSED_PAD src0_sel:WORD_1 src1_sel:DWORD
	v_add3_u32 v16, v16, v19, s71
	v_add3_u32 v17, v17, v18, s71
	v_lshrrev_b32_e32 v16, 16, v16
	v_and_or_b32 v23, v17, s70, v16
	s_andn2_b64 vcc, exec, s[90:91]
	s_cbranch_vccz .LBB0_778
